# stack18 = stack16 + out-projection: first K trip from a literal-zero C operand, the 128 v_mov accumulator zeroing in front of the staging barrier moved to the (unused) skip path
# speedup vs baseline: 1.0027x; 1.0027x over previous
; DEVINL unsigned pk2(float lo, float hi) { const f32x2 v = {lo, hi}; return __builtin_bit_cast(unsigned, __builtin_convertvector(v, bf16v2)); }
; DEVINL float bflo(unsigned u) { return __uint_as_float(u << 16); }
; DEVINL float bfhi(unsigned u) { return __uint_as_float(u & 0xffff0000u); }
; #define LOADB(dst, ks_) do { const unsigned char* ub_ = wb + (size_t)((ks_) * 144) * 1024; \
;         _Pragma("unroll") for (int j_ = 0; j_ < 8; ++j_) dst[j_] = *(const bf16x8*)(ub_ + j_ * 1024 + voff); } while (0)
; #define LOADA(fd, ks_) do { _Pragma("unroll") for (int mi_ = 0; mi_ < 4; ++mi_) fd[mi_] = AFRAG(mi_, ks_); } while (0)
; #define LOADB(dst, ks_) do { const unsigned char* ub_ = wb + (size_t)((ks_) * 64) * 1024; \
;         _Pragma("unroll") for (int j_ = 0; j_ < 8; ++j_) dst[j_] = *(const bf16x8*)(ub_ + j_ * 1024 + voff); } while (0)
; #define LOADA(fd, ks_) do { _Pragma("unroll") for (int mi_ = 0; mi_ < 4; ++mi_) fd[mi_] = AFRAG(mi_, ks_); } while (0)
; DEVINL void phase4(const Params& P, unsigned char* smem) {
;     ...
;             const bf16_t* src = ATT + (size_t)(m0 + row) * DM;
; #pragma unroll 8
;             for (int i = 0; i < 16; ++i) {
;                 const int c = (t & 7) + 8 * i;
;                 u32x4 v = *(const u32x4*)(src + c * 8);
;                 const float sc = (c < 64) ? rna : rsw;
;                 v.x = pk2(bflo(v.x) * sc, bfhi(v.x) * sc); v.y = pk2(bflo(v.y) * sc, bfhi(v.y) * sc);
;                 v.z = pk2(bflo(v.z) * sc, bfhi(v.z) * sc); v.w = pk2(bflo(v.w) * sc, bfhi(v.w) * sc);
;                 *(u32x4*)(smem + row * 2048 + ((c ^ (row & 15)) << 4)) = v;
;             }
;     ...
;             bf16x8 fa[4];
;             LOADB(b0, 0); LOADA(fa, 0);
.LBB0_583:
	s_waitcnt vmcnt(8)
	v_mov_b32_e32 v2, v130
	v_mov_b32_e32 v3, v131
	v_mov_b32_e32 v4, v132
	v_mov_b32_e32 v5, v133
	v_mov_b32_e32 v6, v134
	v_mov_b32_e32 v7, v135
	v_mov_b32_e32 v8, v136
	v_mov_b32_e32 v9, v137
	v_mov_b32_e32 v14, v138
	v_mov_b32_e32 v15, v139
	v_mov_b32_e32 v16, v140
	v_mov_b32_e32 v17, v141
	v_mov_b32_e32 v18, v142
	v_mov_b32_e32 v19, v143
	v_mov_b32_e32 v20, v144
	v_mov_b32_e32 v21, v145
	v_mov_b32_e32 v22, v146
	v_mov_b32_e32 v23, v147
	v_mov_b32_e32 v24, v148
	v_mov_b32_e32 v25, v149
	v_mov_b32_e32 v26, v150
	v_mov_b32_e32 v27, v151
	v_mov_b32_e32 v28, v152
	v_mov_b32_e32 v29, v153
	v_mov_b32_e32 v30, v154
	v_mov_b32_e32 v31, v155
	v_mov_b32_e32 v32, v156
	v_mov_b32_e32 v33, v157
	v_mov_b32_e32 v34, v158
	v_mov_b32_e32 v35, v159
	v_mov_b32_e32 v36, v160
	v_mov_b32_e32 v37, v161
	v_lshlrev_b32_e32 v178, 4, v190
	global_load_dwordx4 v[130:133], v178, s[44:45]
	global_load_dwordx4 v[134:137], v178, s[44:45] offset:1024
	global_load_dwordx4 v[138:141], v178, s[44:45] offset:2048
	global_load_dwordx4 v[142:145], v178, s[44:45] offset:3072
	v_add_u32_e32 v240, 0x1000, v178
	global_load_dwordx4 v[158:161], v240, s[44:45]
	global_load_dwordx4 v[154:157], v240, s[44:45] offset:1024
	global_load_dwordx4 v[150:153], v240, s[44:45] offset:2048
	global_load_dwordx4 v[146:149], v240, s[44:45] offset:3072
	v_add_u32_e32 v39, s0, v218
	s_cmp_eq_u32 s0, 0
	v_xor_b32_e32 v40, v39, v220
	v_add_u32_e32 v41, 8, v39
	v_add_u32_e32 v42, 16, v39
	v_add_u32_e32 v43, 24, v39
	v_add_u32_e32 v44, 32, v39
	s_cselect_b64 vcc, -1, 0
	v_add_u32_e32 v45, 40, v39
	v_add_u32_e32 v46, 48, v39
	v_add_u32_e32 v39, 56, v39
	v_lshl_add_u32 v102, v40, 4, v219
	v_xor_b32_e32 v40, v41, v220
	v_xor_b32_e32 v41, v42, v220
	v_xor_b32_e32 v42, v43, v220
	v_xor_b32_e32 v43, v44, v220
	v_cndmask_b32_e32 v38, v13, v12, vcc
	v_xor_b32_e32 v44, v45, v220
	v_xor_b32_e32 v45, v46, v220
	v_xor_b32_e32 v39, v39, v220
	v_lshl_add_u32 v103, v40, 4, v219
	v_lshl_add_u32 v104, v41, 4, v219
	v_lshl_add_u32 v105, v42, 4, v219
	v_lshl_add_u32 v106, v43, 4, v219
	s_add_i32 s0, s0, 64
	v_lshl_add_u32 v107, v44, 4, v219
	v_lshl_add_u32 v108, v45, 4, v219
	v_lshl_add_u64 v[10:11], v[10:11], 0, s[58:59]
	s_cmpk_eq_i32 s0, 0x80
	v_lshl_add_u32 v109, v39, 4, v219
	v_lshlrev_b32_e32 v40, 16, v2
	v_and_b32_e32 v41, 0xffff0000, v2
	v_lshlrev_b32_e32 v2, 16, v3
	v_and_b32_e32 v3, 0xffff0000, v3
	v_lshlrev_b32_e32 v42, 16, v4
	v_and_b32_e32 v43, 0xffff0000, v4
	v_lshlrev_b32_e32 v4, 16, v5
	v_and_b32_e32 v5, 0xffff0000, v5
	v_lshlrev_b32_e32 v44, 16, v6
	v_and_b32_e32 v45, 0xffff0000, v6
	v_lshlrev_b32_e32 v6, 16, v7
	v_and_b32_e32 v7, 0xffff0000, v7
	v_lshlrev_b32_e32 v46, 16, v8
	v_and_b32_e32 v47, 0xffff0000, v8
	v_lshlrev_b32_e32 v8, 16, v9
	v_and_b32_e32 v9, 0xffff0000, v9
	v_lshlrev_b32_e32 v48, 16, v14
	v_and_b32_e32 v49, 0xffff0000, v14
	v_lshlrev_b32_e32 v14, 16, v15
	v_and_b32_e32 v15, 0xffff0000, v15
	v_lshlrev_b32_e32 v50, 16, v16
	v_and_b32_e32 v51, 0xffff0000, v16
	v_lshlrev_b32_e32 v16, 16, v17
	v_and_b32_e32 v17, 0xffff0000, v17
	v_lshlrev_b32_e32 v52, 16, v18
	v_and_b32_e32 v53, 0xffff0000, v18
	v_lshlrev_b32_e32 v18, 16, v19
	v_and_b32_e32 v19, 0xffff0000, v19
	v_lshlrev_b32_e32 v54, 16, v20
	v_and_b32_e32 v55, 0xffff0000, v20
	v_lshlrev_b32_e32 v20, 16, v21
	v_and_b32_e32 v21, 0xffff0000, v21
	v_lshlrev_b32_e32 v56, 16, v22
	v_and_b32_e32 v57, 0xffff0000, v22
	v_lshlrev_b32_e32 v22, 16, v23
	v_and_b32_e32 v23, 0xffff0000, v23
	v_lshlrev_b32_e32 v58, 16, v24
	v_and_b32_e32 v59, 0xffff0000, v24
	v_lshlrev_b32_e32 v24, 16, v25
	v_and_b32_e32 v25, 0xffff0000, v25
	v_lshlrev_b32_e32 v60, 16, v26
	v_and_b32_e32 v61, 0xffff0000, v26
	v_lshlrev_b32_e32 v26, 16, v27
	v_and_b32_e32 v27, 0xffff0000, v27
	v_lshlrev_b32_e32 v62, 16, v28
	v_and_b32_e32 v63, 0xffff0000, v28
	v_lshlrev_b32_e32 v28, 16, v29
	v_and_b32_e32 v29, 0xffff0000, v29
	v_lshlrev_b32_e32 v64, 16, v30
	v_and_b32_e32 v65, 0xffff0000, v30
	v_lshlrev_b32_e32 v30, 16, v31
	v_and_b32_e32 v31, 0xffff0000, v31
	v_lshlrev_b32_e32 v66, 16, v32
	v_and_b32_e32 v67, 0xffff0000, v32
	v_lshlrev_b32_e32 v32, 16, v33
	v_and_b32_e32 v33, 0xffff0000, v33
	v_lshlrev_b32_e32 v68, 16, v34
	v_and_b32_e32 v69, 0xffff0000, v34
	v_lshlrev_b32_e32 v34, 16, v35
	v_and_b32_e32 v35, 0xffff0000, v35
	v_lshlrev_b32_e32 v70, 16, v36
	v_and_b32_e32 v71, 0xffff0000, v36
	v_lshlrev_b32_e32 v36, 16, v37
	v_and_b32_e32 v37, 0xffff0000, v37
	v_pk_mul_f32 v[40:41], v[38:39], v[40:41] op_sel_hi:[0,1]
	v_pk_mul_f32 v[72:73], v[38:39], v[2:3] op_sel_hi:[0,1]
	v_pk_mul_f32 v[42:43], v[38:39], v[42:43] op_sel_hi:[0,1]
	v_pk_mul_f32 v[74:75], v[38:39], v[4:5] op_sel_hi:[0,1]
	v_pk_mul_f32 v[44:45], v[38:39], v[44:45] op_sel_hi:[0,1]
	v_pk_mul_f32 v[76:77], v[38:39], v[6:7] op_sel_hi:[0,1]
	v_pk_mul_f32 v[46:47], v[38:39], v[46:47] op_sel_hi:[0,1]
	v_pk_mul_f32 v[78:79], v[38:39], v[8:9] op_sel_hi:[0,1]
	v_pk_mul_f32 v[48:49], v[38:39], v[48:49] op_sel_hi:[0,1]
	v_pk_mul_f32 v[80:81], v[38:39], v[14:15] op_sel_hi:[0,1]
	v_pk_mul_f32 v[50:51], v[38:39], v[50:51] op_sel_hi:[0,1]
	v_pk_mul_f32 v[82:83], v[38:39], v[16:17] op_sel_hi:[0,1]
	v_pk_mul_f32 v[52:53], v[38:39], v[52:53] op_sel_hi:[0,1]
	v_pk_mul_f32 v[84:85], v[38:39], v[18:19] op_sel_hi:[0,1]
	v_pk_mul_f32 v[54:55], v[38:39], v[54:55] op_sel_hi:[0,1]
	v_pk_mul_f32 v[86:87], v[38:39], v[20:21] op_sel_hi:[0,1]
	v_pk_mul_f32 v[56:57], v[38:39], v[56:57] op_sel_hi:[0,1]
	v_pk_mul_f32 v[88:89], v[38:39], v[22:23] op_sel_hi:[0,1]
	v_pk_mul_f32 v[58:59], v[38:39], v[58:59] op_sel_hi:[0,1]
	v_pk_mul_f32 v[90:91], v[38:39], v[24:25] op_sel_hi:[0,1]
	v_pk_mul_f32 v[60:61], v[38:39], v[60:61] op_sel_hi:[0,1]
; DEVINL unsigned pk2(float lo, float hi) { const f32x2 v = {lo, hi}; return __builtin_bit_cast(unsigned, __builtin_convertvector(v, bf16v2)); }
; DEVINL float bflo(unsigned u) { return __uint_as_float(u << 16); }
; DEVINL float bfhi(unsigned u) { return __uint_as_float(u & 0xffff0000u); }
; DEVINL void phase4(const Params& P, unsigned char* smem) {
;     ...
;             const bf16_t* src = ATT + (size_t)(m0 + row) * DM;
; #pragma unroll 8
;             for (int i = 0; i < 16; ++i) {
;                 const int c = (t & 7) + 8 * i;
;                 u32x4 v = *(const u32x4*)(src + c * 8);
;                 const float sc = (c < 64) ? rna : rsw;
;                 v.x = pk2(bflo(v.x) * sc, bfhi(v.x) * sc); v.y = pk2(bflo(v.y) * sc, bfhi(v.y) * sc);
;                 v.z = pk2(bflo(v.z) * sc, bfhi(v.z) * sc); v.w = pk2(bflo(v.w) * sc, bfhi(v.w) * sc);
;                 *(u32x4*)(smem + row * 2048 + ((c ^ (row & 15)) << 4)) = v;
;             }
	v_pk_mul_f32 v[92:93], v[38:39], v[26:27] op_sel_hi:[0,1]
	v_pk_mul_f32 v[62:63], v[38:39], v[62:63] op_sel_hi:[0,1]
	v_pk_mul_f32 v[94:95], v[38:39], v[28:29] op_sel_hi:[0,1]
	v_pk_mul_f32 v[64:65], v[38:39], v[64:65] op_sel_hi:[0,1]
	v_pk_mul_f32 v[96:97], v[38:39], v[30:31] op_sel_hi:[0,1]
	v_pk_mul_f32 v[66:67], v[38:39], v[66:67] op_sel_hi:[0,1]
	v_pk_mul_f32 v[98:99], v[38:39], v[32:33] op_sel_hi:[0,1]
	v_pk_mul_f32 v[68:69], v[38:39], v[68:69] op_sel_hi:[0,1]
	v_pk_mul_f32 v[100:101], v[38:39], v[34:35] op_sel_hi:[0,1]
	v_pk_mul_f32 v[70:71], v[38:39], v[70:71] op_sel_hi:[0,1]
	v_pk_mul_f32 v[38:39], v[38:39], v[36:37] op_sel_hi:[0,1]
	v_cvt_pk_bf16_f32 v2, v40, v41
	v_cvt_pk_bf16_f32 v3, v72, v73
	v_cvt_pk_bf16_f32 v4, v42, v43
	v_cvt_pk_bf16_f32 v5, v74, v75
	v_cvt_pk_bf16_f32 v6, v44, v45
	v_cvt_pk_bf16_f32 v7, v76, v77
	v_cvt_pk_bf16_f32 v8, v46, v47
	v_cvt_pk_bf16_f32 v9, v78, v79
	v_cvt_pk_bf16_f32 v14, v48, v49
	v_cvt_pk_bf16_f32 v15, v80, v81
	v_cvt_pk_bf16_f32 v16, v50, v51
	v_cvt_pk_bf16_f32 v17, v82, v83
	v_cvt_pk_bf16_f32 v18, v52, v53
	v_cvt_pk_bf16_f32 v19, v84, v85
	v_cvt_pk_bf16_f32 v20, v54, v55
	v_cvt_pk_bf16_f32 v21, v86, v87
	v_cvt_pk_bf16_f32 v22, v56, v57
	v_cvt_pk_bf16_f32 v23, v88, v89
	v_cvt_pk_bf16_f32 v24, v58, v59
	v_cvt_pk_bf16_f32 v25, v90, v91
	v_cvt_pk_bf16_f32 v26, v60, v61
	v_cvt_pk_bf16_f32 v27, v92, v93
	v_cvt_pk_bf16_f32 v28, v62, v63
	v_cvt_pk_bf16_f32 v29, v94, v95
	v_cvt_pk_bf16_f32 v30, v64, v65
	v_cvt_pk_bf16_f32 v31, v96, v97
	v_cvt_pk_bf16_f32 v32, v66, v67
	v_cvt_pk_bf16_f32 v33, v98, v99
	v_cvt_pk_bf16_f32 v34, v68, v69
	v_cvt_pk_bf16_f32 v35, v100, v101
	v_cvt_pk_bf16_f32 v36, v70, v71
	v_cvt_pk_bf16_f32 v37, v38, v39
	ds_write_b128 v102, v[2:5]
	ds_write_b128 v103, v[6:9]
	ds_write_b128 v104, v[14:17]
	ds_write_b128 v105, v[18:21]
	ds_write_b128 v106, v[22:25]
	ds_write_b128 v107, v[26:29]
	ds_write_b128 v108, v[30:33]
	ds_write_b128 v109, v[34:37]
	s_waitcnt vmcnt(8)
	v_mov_b32_e32 v2, v162
	v_mov_b32_e32 v3, v163
	v_mov_b32_e32 v4, v164
	v_mov_b32_e32 v5, v165
	v_mov_b32_e32 v6, v166
	v_mov_b32_e32 v7, v167
	v_mov_b32_e32 v8, v168
	v_mov_b32_e32 v9, v169
	v_mov_b32_e32 v14, v170
	v_mov_b32_e32 v15, v171
	v_mov_b32_e32 v16, v172
	v_mov_b32_e32 v17, v173
	v_mov_b32_e32 v18, v174
	v_mov_b32_e32 v19, v175
	v_mov_b32_e32 v20, v176
	v_mov_b32_e32 v21, v177
	v_mov_b32_e32 v22, v196
	v_mov_b32_e32 v23, v197
	v_mov_b32_e32 v24, v198
	v_mov_b32_e32 v25, v199
	v_mov_b32_e32 v26, v200
	v_mov_b32_e32 v27, v201
	v_mov_b32_e32 v28, v202
	v_mov_b32_e32 v29, v203
	v_mov_b32_e32 v30, v204
	v_mov_b32_e32 v31, v205
	v_mov_b32_e32 v32, v206
	v_mov_b32_e32 v33, v207
	v_mov_b32_e32 v34, v208
	v_mov_b32_e32 v35, v209
	v_mov_b32_e32 v36, v210
	v_mov_b32_e32 v37, v211
	v_add_u32_e32 v39, s0, v218
	s_cmp_eq_u32 s0, 0
	v_xor_b32_e32 v40, v39, v220
	v_add_u32_e32 v41, 8, v39
	v_add_u32_e32 v42, 16, v39
	v_add_u32_e32 v43, 24, v39
	v_add_u32_e32 v44, 32, v39
	s_cselect_b64 vcc, -1, 0
	v_add_u32_e32 v45, 40, v39
	v_add_u32_e32 v46, 48, v39
	v_add_u32_e32 v39, 56, v39
	v_lshl_add_u32 v102, v40, 4, v219
	v_xor_b32_e32 v40, v41, v220
	v_xor_b32_e32 v41, v42, v220
	v_xor_b32_e32 v42, v43, v220
	v_xor_b32_e32 v43, v44, v220
	v_cndmask_b32_e32 v38, v13, v12, vcc
	v_xor_b32_e32 v44, v45, v220
	v_xor_b32_e32 v45, v46, v220
	v_xor_b32_e32 v39, v39, v220
	v_lshl_add_u32 v103, v40, 4, v219
	v_lshl_add_u32 v104, v41, 4, v219
	v_lshl_add_u32 v105, v42, 4, v219
	v_lshl_add_u32 v106, v43, 4, v219
	s_add_i32 s0, s0, 64
	v_lshl_add_u32 v107, v44, 4, v219
	v_lshl_add_u32 v108, v45, 4, v219
	v_lshl_add_u64 v[10:11], v[10:11], 0, s[58:59]
	s_cmpk_eq_i32 s0, 0x80
	v_lshl_add_u32 v109, v39, 4, v219
	v_lshlrev_b32_e32 v40, 16, v2
	v_and_b32_e32 v41, 0xffff0000, v2
	v_lshlrev_b32_e32 v2, 16, v3
	v_and_b32_e32 v3, 0xffff0000, v3
	v_lshlrev_b32_e32 v42, 16, v4
	v_and_b32_e32 v43, 0xffff0000, v4
	v_lshlrev_b32_e32 v4, 16, v5
	v_and_b32_e32 v5, 0xffff0000, v5
	v_lshlrev_b32_e32 v44, 16, v6
	v_and_b32_e32 v45, 0xffff0000, v6
	v_lshlrev_b32_e32 v6, 16, v7
	v_and_b32_e32 v7, 0xffff0000, v7
	v_lshlrev_b32_e32 v46, 16, v8
	v_and_b32_e32 v47, 0xffff0000, v8
	v_lshlrev_b32_e32 v8, 16, v9
	v_and_b32_e32 v9, 0xffff0000, v9
	v_lshlrev_b32_e32 v48, 16, v14
	v_and_b32_e32 v49, 0xffff0000, v14
	v_lshlrev_b32_e32 v14, 16, v15
	v_and_b32_e32 v15, 0xffff0000, v15
	v_lshlrev_b32_e32 v50, 16, v16
	v_and_b32_e32 v51, 0xffff0000, v16
	v_lshlrev_b32_e32 v16, 16, v17
	v_and_b32_e32 v17, 0xffff0000, v17
	v_lshlrev_b32_e32 v52, 16, v18
	v_and_b32_e32 v53, 0xffff0000, v18
	v_lshlrev_b32_e32 v18, 16, v19
	v_and_b32_e32 v19, 0xffff0000, v19
	v_lshlrev_b32_e32 v54, 16, v20
	v_and_b32_e32 v55, 0xffff0000, v20
	v_lshlrev_b32_e32 v20, 16, v21
	v_and_b32_e32 v21, 0xffff0000, v21
	v_lshlrev_b32_e32 v56, 16, v22
	v_and_b32_e32 v57, 0xffff0000, v22
	v_lshlrev_b32_e32 v22, 16, v23
	v_and_b32_e32 v23, 0xffff0000, v23
	v_lshlrev_b32_e32 v58, 16, v24
	v_and_b32_e32 v59, 0xffff0000, v24
	v_lshlrev_b32_e32 v24, 16, v25
	v_and_b32_e32 v25, 0xffff0000, v25
	v_lshlrev_b32_e32 v60, 16, v26
	v_and_b32_e32 v61, 0xffff0000, v26
	v_lshlrev_b32_e32 v26, 16, v27
	v_and_b32_e32 v27, 0xffff0000, v27
	v_lshlrev_b32_e32 v62, 16, v28
	v_and_b32_e32 v63, 0xffff0000, v28
	v_lshlrev_b32_e32 v28, 16, v29
	v_and_b32_e32 v29, 0xffff0000, v29
	v_lshlrev_b32_e32 v64, 16, v30
	v_and_b32_e32 v65, 0xffff0000, v30
	v_lshlrev_b32_e32 v30, 16, v31
	v_and_b32_e32 v31, 0xffff0000, v31
	v_lshlrev_b32_e32 v66, 16, v32
	v_and_b32_e32 v67, 0xffff0000, v32
	v_lshlrev_b32_e32 v32, 16, v33
	v_and_b32_e32 v33, 0xffff0000, v33
	v_lshlrev_b32_e32 v68, 16, v34
	v_and_b32_e32 v69, 0xffff0000, v34
	v_lshlrev_b32_e32 v34, 16, v35
; #define LOADB(dst, ks_) do { const unsigned char* ub_ = wb + (size_t)((ks_) * 144) * 1024; \
;         _Pragma("unroll") for (int j_ = 0; j_ < 8; ++j_) dst[j_] = *(const bf16x8*)(ub_ + j_ * 1024 + voff); } while (0)
; #define LOADA(fd, ks_) do { _Pragma("unroll") for (int mi_ = 0; mi_ < 4; ++mi_) fd[mi_] = AFRAG(mi_, ks_); } while (0)
; #define MMA(src, fs, ksn_) do { _Pragma("unroll") for (int mi_ = 0; mi_ < 4; ++mi_) { \
;         _Pragma("unroll") for (int j_ = 0; j_ < 8; ++j_) acc[j_][mi_] = __builtin_amdgcn_mfma_f32_16x16x32_bf16(src[j_], fs[mi_], acc[j_][mi_], 0, 0, 0); \
;         fs[mi_] = AFRAG(mi_, (ksn_) < 32 ? (ksn_) : 31); } } while (0)
; #define LOADB(dst, ks_) do { const unsigned char* ub_ = wb + (size_t)((ks_) * 64) * 1024; \
;         _Pragma("unroll") for (int j_ = 0; j_ < 8; ++j_) dst[j_] = *(const bf16x8*)(ub_ + j_ * 1024 + voff); } while (0)
; #define LOADA(fd, ks_) do { _Pragma("unroll") for (int mi_ = 0; mi_ < 4; ++mi_) fd[mi_] = AFRAG(mi_, ks_); } while (0)
; #define MMA(src, fs, ksn_) do { _Pragma("unroll") for (int mi_ = 0; mi_ < 4; ++mi_) { \
;         _Pragma("unroll") for (int j_ = 0; j_ < 8; ++j_) acc[j_][mi_] = __builtin_amdgcn_mfma_f32_16x16x32_bf16(src[j_], fs[mi_], acc[j_][mi_], 0, 0, 0); \
;         fs[mi_] = AFRAG(mi_, (ksn_) < 32 ? (ksn_) : 31); } } while (0)
; DEVINL void phase4(const Params& P, unsigned char* smem) {
;     ...
;                 *(u32x4*)(smem + row * 2048 + ((c ^ (row & 15)) << 4)) = v;
;             }
;         }
;         __syncthreads();
;         f32x4 acc[8][4];
; #pragma unroll
;         for (int i = 0; i < 8; ++i)
; #pragma unroll
;             for (int mi = 0; mi < 4; ++mi) acc[i][mi] = (f32x4){0.f, 0.f, 0.f, 0.f};
;         if (!SKIPF(32)) {
;             const unsigned char* wb = (const unsigned char*)(P.ws + WS_WOF) + (size_t)(8 * wv) * 1024;
;             unsigned voff = (unsigned)(lane * 16);
;             asm volatile("" : "+v"(voff));
;             const int aoff = lr * 2048;
;     ...
;             bf16x8 b0[8], b1[8];
;     ...
;             bf16x8 fa[4];
;             LOADB(b0, 0); LOADA(fa, 0);
; #pragma unroll 1
;             for (int ks = 0; ks < 32; ks += 2) {
;                 LOADB(b1, ks + 1);
;                 __builtin_amdgcn_sched_barrier(0);
;                 MMA(b0, fa, ks + 1);
	v_and_b32_e32 v35, 0xffff0000, v35
	v_lshlrev_b32_e32 v70, 16, v36
	v_and_b32_e32 v71, 0xffff0000, v36
	v_lshlrev_b32_e32 v36, 16, v37
	v_and_b32_e32 v37, 0xffff0000, v37
	v_pk_mul_f32 v[40:41], v[38:39], v[40:41] op_sel_hi:[0,1]
	v_pk_mul_f32 v[72:73], v[38:39], v[2:3] op_sel_hi:[0,1]
	v_pk_mul_f32 v[42:43], v[38:39], v[42:43] op_sel_hi:[0,1]
	v_pk_mul_f32 v[74:75], v[38:39], v[4:5] op_sel_hi:[0,1]
	v_pk_mul_f32 v[44:45], v[38:39], v[44:45] op_sel_hi:[0,1]
	v_pk_mul_f32 v[76:77], v[38:39], v[6:7] op_sel_hi:[0,1]
	v_pk_mul_f32 v[46:47], v[38:39], v[46:47] op_sel_hi:[0,1]
	v_pk_mul_f32 v[78:79], v[38:39], v[8:9] op_sel_hi:[0,1]
	v_pk_mul_f32 v[48:49], v[38:39], v[48:49] op_sel_hi:[0,1]
	v_pk_mul_f32 v[80:81], v[38:39], v[14:15] op_sel_hi:[0,1]
	v_pk_mul_f32 v[50:51], v[38:39], v[50:51] op_sel_hi:[0,1]
	v_pk_mul_f32 v[82:83], v[38:39], v[16:17] op_sel_hi:[0,1]
	v_pk_mul_f32 v[52:53], v[38:39], v[52:53] op_sel_hi:[0,1]
	v_pk_mul_f32 v[84:85], v[38:39], v[18:19] op_sel_hi:[0,1]
	v_pk_mul_f32 v[54:55], v[38:39], v[54:55] op_sel_hi:[0,1]
	v_pk_mul_f32 v[86:87], v[38:39], v[20:21] op_sel_hi:[0,1]
	v_pk_mul_f32 v[56:57], v[38:39], v[56:57] op_sel_hi:[0,1]
	v_pk_mul_f32 v[88:89], v[38:39], v[22:23] op_sel_hi:[0,1]
	v_pk_mul_f32 v[58:59], v[38:39], v[58:59] op_sel_hi:[0,1]
	v_pk_mul_f32 v[90:91], v[38:39], v[24:25] op_sel_hi:[0,1]
	v_pk_mul_f32 v[60:61], v[38:39], v[60:61] op_sel_hi:[0,1]
	v_pk_mul_f32 v[92:93], v[38:39], v[26:27] op_sel_hi:[0,1]
	v_pk_mul_f32 v[62:63], v[38:39], v[62:63] op_sel_hi:[0,1]
	v_pk_mul_f32 v[94:95], v[38:39], v[28:29] op_sel_hi:[0,1]
	v_pk_mul_f32 v[64:65], v[38:39], v[64:65] op_sel_hi:[0,1]
	v_pk_mul_f32 v[96:97], v[38:39], v[30:31] op_sel_hi:[0,1]
	v_pk_mul_f32 v[66:67], v[38:39], v[66:67] op_sel_hi:[0,1]
	v_pk_mul_f32 v[98:99], v[38:39], v[32:33] op_sel_hi:[0,1]
	v_pk_mul_f32 v[68:69], v[38:39], v[68:69] op_sel_hi:[0,1]
	v_pk_mul_f32 v[100:101], v[38:39], v[34:35] op_sel_hi:[0,1]
	v_pk_mul_f32 v[70:71], v[38:39], v[70:71] op_sel_hi:[0,1]
	v_pk_mul_f32 v[38:39], v[38:39], v[36:37] op_sel_hi:[0,1]
	v_cvt_pk_bf16_f32 v2, v40, v41
	v_cvt_pk_bf16_f32 v3, v72, v73
	v_cvt_pk_bf16_f32 v4, v42, v43
	v_cvt_pk_bf16_f32 v5, v74, v75
	v_cvt_pk_bf16_f32 v6, v44, v45
	v_cvt_pk_bf16_f32 v7, v76, v77
	v_cvt_pk_bf16_f32 v8, v46, v47
	v_cvt_pk_bf16_f32 v9, v78, v79
	v_cvt_pk_bf16_f32 v14, v48, v49
	v_cvt_pk_bf16_f32 v15, v80, v81
	v_cvt_pk_bf16_f32 v16, v50, v51
	v_cvt_pk_bf16_f32 v17, v82, v83
	v_cvt_pk_bf16_f32 v18, v52, v53
	v_cvt_pk_bf16_f32 v19, v84, v85
	v_cvt_pk_bf16_f32 v20, v54, v55
	v_cvt_pk_bf16_f32 v21, v86, v87
	v_cvt_pk_bf16_f32 v22, v56, v57
	v_cvt_pk_bf16_f32 v23, v88, v89
	v_cvt_pk_bf16_f32 v24, v58, v59
	v_cvt_pk_bf16_f32 v25, v90, v91
	v_cvt_pk_bf16_f32 v26, v60, v61
	v_cvt_pk_bf16_f32 v27, v92, v93
	v_cvt_pk_bf16_f32 v28, v62, v63
	v_cvt_pk_bf16_f32 v29, v94, v95
	v_cvt_pk_bf16_f32 v30, v64, v65
	v_cvt_pk_bf16_f32 v31, v96, v97
	v_cvt_pk_bf16_f32 v32, v66, v67
	v_cvt_pk_bf16_f32 v33, v98, v99
	v_cvt_pk_bf16_f32 v34, v68, v69
	v_cvt_pk_bf16_f32 v35, v100, v101
	v_cvt_pk_bf16_f32 v36, v70, v71
	v_cvt_pk_bf16_f32 v37, v38, v39
	ds_write_b128 v102, v[2:5]
	ds_write_b128 v103, v[6:9]
	ds_write_b128 v104, v[14:17]
	ds_write_b128 v105, v[18:21]
	ds_write_b128 v106, v[22:25]
	ds_write_b128 v107, v[26:29]
	ds_write_b128 v108, v[30:33]
	ds_write_b128 v109, v[34:37]
	v_and_b32_e32 v238, 15, v190
	v_ashrrev_i32_e32 v204, 4, v190
	s_and_b64 vcc, exec, s[42:43]
	s_waitcnt lgkmcnt(0)
	s_barrier
	s_cbranch_vccz .Lp4_zskip
	v_lshl_add_u64 v[192:193], s[44:45], 0, v[178:179]
	v_lshl_add_u32 v191, v238, 11, 0
	v_xor_b32_e32 v2, v204, v238
	v_lshl_add_u32 v2, v2, 4, v191
	v_add_u32_e32 v3, 0x10000, v2
	ds_read_b128 v[174:177], v2
	ds_read_b128 v[170:173], v2 offset:32768
	v_add_u32_e32 v2, 0x18000, v2
	ds_read_b128 v[166:169], v3
	ds_read_b128 v[162:165], v2
	s_mov_b32 s0, 0
	v_add_u32_e32 v196, 4, v204
	v_lshl_add_u64 v[194:195], s[52:53], 0, v[178:179]
	s_mov_b64 s[8:9], 0x1000
	v_lshl_add_u64 v[194:195], v[194:195], 0, s[8:9]
	global_load_dwordx4 v[198:201], v[194:195], off offset:-4096
	global_load_dwordx4 v[206:209], v[194:195], off offset:-3072
	global_load_dwordx4 v[210:213], v[194:195], off offset:-2048
	global_load_dwordx4 v[240:243], v[194:195], off offset:-1024
	global_load_dwordx4 v[244:247], v[194:195], off
	global_load_dwordx4 v[248:251], v[194:195], off offset:1024
	global_load_dwordx4 v[226:229], v[194:195], off offset:2048
	global_load_dwordx4 v[230:233], v[194:195], off offset:3072
	s_add_i32 s1, s0, 2
	s_lshl_b32 s24, s1, 16
	s_add_i32 s24, s24, 0x1000
	v_xor_b32_e32 v236, v196, v238
	v_lshl_add_u32 v236, v236, 4, v191
	v_add_u32_e32 v237, 0x10000, v236
	v_lshl_add_u64 v[234:235], v[192:193], 0, s[24:25]
	s_waitcnt vmcnt(15) lgkmcnt(3)
	v_mfma_f32_16x16x32_bf16 v[126:129], v[130:133], v[174:177], 0
	s_waitcnt lgkmcnt(2)
	v_mfma_f32_16x16x32_bf16 v[122:125], v[130:133], v[170:173], 0
	s_waitcnt vmcnt(14)
	v_mfma_f32_16x16x32_bf16 v[118:121], v[134:137], v[174:177], 0
	v_mfma_f32_16x16x32_bf16 v[114:117], v[134:137], v[170:173], 0
	s_waitcnt vmcnt(13)
	v_mfma_f32_16x16x32_bf16 v[110:113], v[138:141], v[174:177], 0
	v_mfma_f32_16x16x32_bf16 v[106:109], v[138:141], v[170:173], 0
	s_waitcnt vmcnt(12)
	v_mfma_f32_16x16x32_bf16 v[102:105], v[142:145], v[174:177], 0
	v_mfma_f32_16x16x32_bf16 v[98:101], v[142:145], v[170:173], 0
	s_waitcnt vmcnt(11)
	v_mfma_f32_16x16x32_bf16 v[94:97], v[158:161], v[174:177], 0
	v_mfma_f32_16x16x32_bf16 v[90:93], v[158:161], v[170:173], 0
	s_waitcnt vmcnt(10)
; #define LOADB(dst, ks_) do { const unsigned char* ub_ = wb + (size_t)((ks_) * 144) * 1024; \
;         _Pragma("unroll") for (int j_ = 0; j_ < 8; ++j_) dst[j_] = *(const bf16x8*)(ub_ + j_ * 1024 + voff); } while (0)
; #define LOADA(fd, ks_) do { _Pragma("unroll") for (int mi_ = 0; mi_ < 4; ++mi_) fd[mi_] = AFRAG(mi_, ks_); } while (0)
; #define MMA(src, fs, ksn_) do { _Pragma("unroll") for (int mi_ = 0; mi_ < 4; ++mi_) { \
;         _Pragma("unroll") for (int j_ = 0; j_ < 8; ++j_) acc[j_][mi_] = __builtin_amdgcn_mfma_f32_16x16x32_bf16(src[j_], fs[mi_], acc[j_][mi_], 0, 0, 0); \
;         fs[mi_] = AFRAG(mi_, (ksn_) < 32 ? (ksn_) : 31); } } while (0)
; #define LOADB(dst, ks_) do { const unsigned char* ub_ = wb + (size_t)((ks_) * 64) * 1024; \
;         _Pragma("unroll") for (int j_ = 0; j_ < 8; ++j_) dst[j_] = *(const bf16x8*)(ub_ + j_ * 1024 + voff); } while (0)
; #define LOADA(fd, ks_) do { _Pragma("unroll") for (int mi_ = 0; mi_ < 4; ++mi_) fd[mi_] = AFRAG(mi_, ks_); } while (0)
; #define MMA(src, fs, ksn_) do { _Pragma("unroll") for (int mi_ = 0; mi_ < 4; ++mi_) { \
;         _Pragma("unroll") for (int j_ = 0; j_ < 8; ++j_) acc[j_][mi_] = __builtin_amdgcn_mfma_f32_16x16x32_bf16(src[j_], fs[mi_], acc[j_][mi_], 0, 0, 0); \
;         fs[mi_] = AFRAG(mi_, (ksn_) < 32 ? (ksn_) : 31); } } while (0)
; DEVINL void phase4(const Params& P, unsigned char* smem) {
;     ...
;             bf16x8 fa[4];
;             LOADB(b0, 0); LOADA(fa, 0);
; #pragma unroll 1
;             for (int ks = 0; ks < 32; ks += 2) {
;                 LOADB(b1, ks + 1);
;                 __builtin_amdgcn_sched_barrier(0);
;                 MMA(b0, fa, ks + 1);
;                 __builtin_amdgcn_sched_barrier(0);
;                 LOADB(b0, ks + 2 < 32 ? ks + 2 : 31);
;                 __builtin_amdgcn_sched_barrier(0);
;                 MMA(b1, fa, ks + 2);
;                 __builtin_amdgcn_sched_barrier(0);
;             }
	v_mfma_f32_16x16x32_bf16 v[86:89], v[154:157], v[174:177], 0
	v_mfma_f32_16x16x32_bf16 v[82:85], v[154:157], v[170:173], 0
	s_waitcnt vmcnt(9)
	v_mfma_f32_16x16x32_bf16 v[78:81], v[150:153], v[174:177], 0
	v_mfma_f32_16x16x32_bf16 v[74:77], v[150:153], v[170:173], 0
	s_waitcnt vmcnt(8)
	v_mfma_f32_16x16x32_bf16 v[70:73], v[146:149], v[174:177], 0
	v_mfma_f32_16x16x32_bf16 v[66:69], v[146:149], v[170:173], 0
	s_waitcnt lgkmcnt(1)
	v_mfma_f32_16x16x32_bf16 v[62:65], v[130:133], v[166:169], 0
	s_waitcnt lgkmcnt(0)
	v_mfma_f32_16x16x32_bf16 v[58:61], v[130:133], v[162:165], 0
	global_load_dwordx4 v[130:133], v[234:235], off offset:-4096
	v_mfma_f32_16x16x32_bf16 v[54:57], v[134:137], v[166:169], 0
	v_mfma_f32_16x16x32_bf16 v[50:53], v[134:137], v[162:165], 0
	global_load_dwordx4 v[134:137], v[234:235], off offset:-3072
	ds_read_b128 v[174:177], v236
	v_mfma_f32_16x16x32_bf16 v[46:49], v[138:141], v[166:169], 0
	v_mfma_f32_16x16x32_bf16 v[42:45], v[138:141], v[162:165], 0
	global_load_dwordx4 v[138:141], v[234:235], off offset:-2048
	ds_read_b128 v[170:173], v236 offset:32768
	v_mfma_f32_16x16x32_bf16 v[38:41], v[142:145], v[166:169], 0
	v_mfma_f32_16x16x32_bf16 v[34:37], v[142:145], v[162:165], 0
	global_load_dwordx4 v[142:145], v[234:235], off offset:-1024
	v_mfma_f32_16x16x32_bf16 v[30:33], v[158:161], v[166:169], 0
	v_mfma_f32_16x16x32_bf16 v[26:29], v[158:161], v[162:165], 0
	global_load_dwordx4 v[158:161], v[234:235], off
	v_mfma_f32_16x16x32_bf16 v[22:25], v[154:157], v[166:169], 0
	v_mfma_f32_16x16x32_bf16 v[18:21], v[154:157], v[162:165], 0
	global_load_dwordx4 v[154:157], v[234:235], off offset:1024
	v_mfma_f32_16x16x32_bf16 v[14:17], v[150:153], v[166:169], 0
	v_mfma_f32_16x16x32_bf16 v[10:13], v[150:153], v[162:165], 0
	global_load_dwordx4 v[150:153], v[234:235], off offset:2048
	v_mfma_f32_16x16x32_bf16 v[6:9], v[146:149], v[166:169], 0
	v_mfma_f32_16x16x32_bf16 v[2:5], v[146:149], v[162:165], 0
	global_load_dwordx4 v[146:149], v[234:235], off offset:3072
	ds_read_b128 v[166:169], v237
	ds_read_b128 v[162:165], v237 offset:32768
	v_lshl_add_u32 v236, s1, 2, v204
	v_lshl_add_u64 v[194:195], v[194:195], 0, s[60:61]
	v_xor_b32_e32 v236, v236, v238
	v_lshl_add_u32 v236, v236, 4, v191
	v_add_u32_e32 v237, 0x10000, v236
	s_waitcnt vmcnt(15) lgkmcnt(3)
	v_mfma_f32_16x16x32_bf16 v[126:129], v[198:201], v[174:177], v[126:129]
	s_waitcnt lgkmcnt(2)
	v_mfma_f32_16x16x32_bf16 v[122:125], v[198:201], v[170:173], v[122:125]
	s_waitcnt vmcnt(14)
	v_mfma_f32_16x16x32_bf16 v[118:121], v[206:209], v[174:177], v[118:121]
	v_mfma_f32_16x16x32_bf16 v[114:117], v[206:209], v[170:173], v[114:117]
	s_waitcnt vmcnt(13)
	v_mfma_f32_16x16x32_bf16 v[110:113], v[210:213], v[174:177], v[110:113]
	v_mfma_f32_16x16x32_bf16 v[106:109], v[210:213], v[170:173], v[106:109]
	s_waitcnt vmcnt(12)
	v_mfma_f32_16x16x32_bf16 v[102:105], v[240:243], v[174:177], v[102:105]
	v_mfma_f32_16x16x32_bf16 v[98:101], v[240:243], v[170:173], v[98:101]
	s_waitcnt vmcnt(11)
	v_mfma_f32_16x16x32_bf16 v[94:97], v[244:247], v[174:177], v[94:97]
	v_mfma_f32_16x16x32_bf16 v[90:93], v[244:247], v[170:173], v[90:93]
	s_waitcnt vmcnt(10)
	v_mfma_f32_16x16x32_bf16 v[86:89], v[248:251], v[174:177], v[86:89]
	v_mfma_f32_16x16x32_bf16 v[82:85], v[248:251], v[170:173], v[82:85]
	s_waitcnt vmcnt(9)
	v_mfma_f32_16x16x32_bf16 v[78:81], v[226:229], v[174:177], v[78:81]
	v_mfma_f32_16x16x32_bf16 v[74:77], v[226:229], v[170:173], v[74:77]
	s_waitcnt vmcnt(8)
	v_mfma_f32_16x16x32_bf16 v[70:73], v[230:233], v[174:177], v[70:73]
	v_mfma_f32_16x16x32_bf16 v[66:69], v[230:233], v[170:173], v[66:69]
	s_waitcnt lgkmcnt(1)
	v_mfma_f32_16x16x32_bf16 v[62:65], v[198:201], v[166:169], v[62:65]
	s_waitcnt lgkmcnt(0)
	v_mfma_f32_16x16x32_bf16 v[58:61], v[198:201], v[162:165], v[58:61]
	global_load_dwordx4 v[198:201], v[194:195], off offset:-4096
	v_mfma_f32_16x16x32_bf16 v[54:57], v[206:209], v[166:169], v[54:57]
	v_mfma_f32_16x16x32_bf16 v[50:53], v[206:209], v[162:165], v[50:53]
	global_load_dwordx4 v[206:209], v[194:195], off offset:-3072
	ds_read_b128 v[174:177], v236
	v_mfma_f32_16x16x32_bf16 v[46:49], v[210:213], v[166:169], v[46:49]
	v_mfma_f32_16x16x32_bf16 v[42:45], v[210:213], v[162:165], v[42:45]
	global_load_dwordx4 v[210:213], v[194:195], off offset:-2048
	ds_read_b128 v[170:173], v236 offset:32768
	v_mfma_f32_16x16x32_bf16 v[38:41], v[240:243], v[166:169], v[38:41]
	v_mfma_f32_16x16x32_bf16 v[34:37], v[240:243], v[162:165], v[34:37]
	global_load_dwordx4 v[240:243], v[194:195], off offset:-1024
	v_mfma_f32_16x16x32_bf16 v[30:33], v[244:247], v[166:169], v[30:33]
	v_mfma_f32_16x16x32_bf16 v[26:29], v[244:247], v[162:165], v[26:29]
	global_load_dwordx4 v[244:247], v[194:195], off
	v_mfma_f32_16x16x32_bf16 v[22:25], v[248:251], v[166:169], v[22:25]
	v_mfma_f32_16x16x32_bf16 v[18:21], v[248:251], v[162:165], v[18:21]
	global_load_dwordx4 v[248:251], v[194:195], off offset:1024
	v_mfma_f32_16x16x32_bf16 v[14:17], v[226:229], v[166:169], v[14:17]
	v_mfma_f32_16x16x32_bf16 v[10:13], v[226:229], v[162:165], v[10:13]
	global_load_dwordx4 v[226:229], v[194:195], off offset:2048
	v_mfma_f32_16x16x32_bf16 v[6:9], v[230:233], v[166:169], v[6:9]
	v_mfma_f32_16x16x32_bf16 v[2:5], v[230:233], v[162:165], v[2:5]
	global_load_dwordx4 v[230:233], v[194:195], off offset:3072
	ds_read_b128 v[166:169], v237
	ds_read_b128 v[162:165], v237 offset:32768
	v_add_u32_e32 v196, 8, v196
	s_mov_b32 s0, s1

; DEVINL void phase4(const Params& P, unsigned char* smem) {
;     ...
;         f32x4 acc[8][4];
; #pragma unroll
;         for (int i = 0; i < 8; ++i)
; #pragma unroll
;             for (int mi = 0; mi < 4; ++mi) acc[i][mi] = (f32x4){0.f, 0.f, 0.f, 0.f};
;         if (!SKIPF(32)) {
.Lp4_zskip:
	v_mov_b32_e32 v5, 0
	v_mov_b32_e32 v4, v5
	v_mov_b32_e32 v3, v5
	v_mov_b32_e32 v2, v5
	v_mov_b32_e32 v9, v5
	v_mov_b32_e32 v8, v5
	v_mov_b32_e32 v7, v5
	v_mov_b32_e32 v6, v5
	v_mov_b32_e32 v69, v5
	v_mov_b32_e32 v68, v5
	v_mov_b32_e32 v67, v5
	v_mov_b32_e32 v66, v5
	v_mov_b32_e32 v73, v5
	v_mov_b32_e32 v72, v5
	v_mov_b32_e32 v71, v5
	v_mov_b32_e32 v70, v5
	v_mov_b32_e32 v13, v5
	v_mov_b32_e32 v12, v5
	v_mov_b32_e32 v11, v5
	v_mov_b32_e32 v10, v5
	v_mov_b32_e32 v17, v5
	v_mov_b32_e32 v16, v5
	v_mov_b32_e32 v15, v5
	v_mov_b32_e32 v14, v5
	v_mov_b32_e32 v77, v5
	v_mov_b32_e32 v76, v5
	v_mov_b32_e32 v75, v5
	v_mov_b32_e32 v74, v5
	v_mov_b32_e32 v81, v5
	v_mov_b32_e32 v80, v5
	v_mov_b32_e32 v79, v5
	v_mov_b32_e32 v78, v5
	v_mov_b32_e32 v21, v5
	v_mov_b32_e32 v20, v5
	v_mov_b32_e32 v19, v5
	v_mov_b32_e32 v18, v5
	v_mov_b32_e32 v25, v5
	v_mov_b32_e32 v24, v5
	v_mov_b32_e32 v23, v5
	v_mov_b32_e32 v22, v5
	v_mov_b32_e32 v85, v5
	v_mov_b32_e32 v84, v5
	v_mov_b32_e32 v83, v5
	v_mov_b32_e32 v82, v5
	v_mov_b32_e32 v89, v5
	v_mov_b32_e32 v88, v5
	v_mov_b32_e32 v87, v5
	v_mov_b32_e32 v86, v5
	v_mov_b32_e32 v29, v5
	v_mov_b32_e32 v28, v5
	v_mov_b32_e32 v27, v5
	v_mov_b32_e32 v26, v5
	v_mov_b32_e32 v33, v5
	v_mov_b32_e32 v32, v5
	v_mov_b32_e32 v31, v5
	v_mov_b32_e32 v30, v5
	v_mov_b32_e32 v93, v5
	v_mov_b32_e32 v92, v5
	v_mov_b32_e32 v91, v5
	v_mov_b32_e32 v90, v5
	v_mov_b32_e32 v97, v5
	v_mov_b32_e32 v96, v5
	v_mov_b32_e32 v95, v5
	v_mov_b32_e32 v94, v5
	v_mov_b32_e32 v129, v5
	v_mov_b32_e32 v128, v5
	v_mov_b32_e32 v127, v5
	v_mov_b32_e32 v126, v5
	v_mov_b32_e32 v125, v5
	v_mov_b32_e32 v124, v5
	v_mov_b32_e32 v123, v5
	v_mov_b32_e32 v122, v5
	v_mov_b32_e32 v65, v5
	v_mov_b32_e32 v64, v5
	v_mov_b32_e32 v63, v5
	v_mov_b32_e32 v62, v5
	v_mov_b32_e32 v61, v5
	v_mov_b32_e32 v60, v5
	v_mov_b32_e32 v59, v5
	v_mov_b32_e32 v58, v5
	v_mov_b32_e32 v121, v5
	v_mov_b32_e32 v120, v5
	v_mov_b32_e32 v119, v5
	v_mov_b32_e32 v118, v5
	v_mov_b32_e32 v117, v5
	v_mov_b32_e32 v116, v5
	v_mov_b32_e32 v115, v5
	v_mov_b32_e32 v114, v5
	v_mov_b32_e32 v57, v5
	v_mov_b32_e32 v56, v5
	v_mov_b32_e32 v55, v5
	v_mov_b32_e32 v54, v5
	v_mov_b32_e32 v53, v5
	v_mov_b32_e32 v52, v5
	v_mov_b32_e32 v51, v5
	v_mov_b32_e32 v50, v5
	v_mov_b32_e32 v113, v5
	v_mov_b32_e32 v112, v5
	v_mov_b32_e32 v111, v5
	v_mov_b32_e32 v110, v5
	v_mov_b32_e32 v109, v5
	v_mov_b32_e32 v108, v5
	v_mov_b32_e32 v107, v5
	v_mov_b32_e32 v106, v5
	v_mov_b32_e32 v49, v5
	v_mov_b32_e32 v48, v5
	v_mov_b32_e32 v47, v5
	v_mov_b32_e32 v46, v5
	v_mov_b32_e32 v45, v5
	v_mov_b32_e32 v44, v5
	v_mov_b32_e32 v43, v5
	v_mov_b32_e32 v42, v5
	v_mov_b32_e32 v105, v5
	v_mov_b32_e32 v104, v5
	v_mov_b32_e32 v103, v5
	v_mov_b32_e32 v102, v5
	v_mov_b32_e32 v101, v5
	v_mov_b32_e32 v100, v5
	v_mov_b32_e32 v99, v5
	v_mov_b32_e32 v98, v5
	v_mov_b32_e32 v41, v5
	v_mov_b32_e32 v40, v5
	v_mov_b32_e32 v39, v5
	v_mov_b32_e32 v38, v5
	v_mov_b32_e32 v37, v5
	v_mov_b32_e32 v36, v5
	v_mov_b32_e32 v35, v5
	v_mov_b32_e32 v34, v5
	s_branch .LBB0_587
